# speedup vs baseline: 1.0152x; 1.0152x over previous
.LBB1_4:
	v_add_u32_e32 v182, s19, v191
	v_add_u32_e32 v238, s19, v192
	ds_read_b128 v[178:181], v182 offset:32768
	ds_read_b128 v[194:197], v182 offset:34816
	ds_read_b128 v[198:201], v182 offset:36864
	ds_read_b128 v[202:205], v182 offset:38912
	ds_read_b128 v[206:209], v238
	ds_read_b128 v[210:213], v238 offset:2048
	ds_read_b128 v[214:217], v238 offset:4096
	ds_read_b128 v[218:221], v238 offset:6144
	ds_read_b128 v[222:225], v238 offset:8192
	ds_read_b128 v[226:229], v238 offset:10240
	ds_read_b128 v[230:233], v238 offset:12288
	ds_read_b128 v[234:237], v238 offset:14336
	s_min_u32 s21, s20, 29
	s_xor_b32 s19, s19, 0x10000
	v_add_u32_e32 v239, s19, v189
	s_waitcnt vmcnt(11)
	v_cvt_pk_bf16_f32 v13, v12, v13
	v_cvt_pk_bf16_f32 v12, v10, v11
	s_waitcnt vmcnt(10)
	v_cvt_pk_bf16_f32 v11, v20, v21
	v_cvt_pk_bf16_f32 v10, v18, v19
	ds_write2st64_b64 v239, v[12:13], v[10:11] offset1:8
	s_waitcnt vmcnt(9)
	v_cvt_pk_bf16_f32 v11, v24, v25
	v_cvt_pk_bf16_f32 v10, v22, v23
	s_waitcnt vmcnt(8)
	v_cvt_pk_bf16_f32 v13, v32, v33
	v_cvt_pk_bf16_f32 v12, v30, v31
	ds_write2st64_b64 v239, v[10:11], v[12:13] offset0:16 offset1:24
	s_waitcnt vmcnt(7)
	v_cvt_pk_bf16_f32 v11, v36, v37
	v_cvt_pk_bf16_f32 v10, v34, v35
	s_waitcnt vmcnt(6)
	v_cvt_pk_bf16_f32 v13, v40, v41
	v_cvt_pk_bf16_f32 v12, v38, v39
	ds_write2st64_b64 v239, v[10:11], v[12:13] offset0:32 offset1:40
	s_waitcnt vmcnt(5)
	v_cvt_pk_bf16_f32 v11, v44, v45
	v_cvt_pk_bf16_f32 v10, v42, v43
	s_waitcnt vmcnt(4)
	v_cvt_pk_bf16_f32 v13, v48, v49
	v_cvt_pk_bf16_f32 v12, v46, v47
	ds_write2st64_b64 v239, v[10:11], v[12:13] offset0:48 offset1:56
	s_waitcnt lgkmcnt(0)
	s_add_i32 s21, s21, 2
	s_barrier
	v_mfma_f32_16x16x32_bf16 v[174:177], v[178:181], v[206:209], v[174:177]
	s_lshl_b32 s22, s21, 1
	s_and_b32 s22, s22, 0x60
	s_add_i32 s22, s22, s12
	s_lshl_b32 s22, s22, 6
	v_mfma_f32_16x16x32_bf16 v[170:173], v[194:197], v[206:209], v[170:173]
	s_and_b32 s22, s22, 0x3f00
	s_or_b32 s22, s22, s13
	s_lshl_b32 s23, s21, 23
	s_lshl_b32 s22, s22, 9
	v_mfma_f32_16x16x32_bf16 v[158:161], v[198:201], v[206:209], v[158:161]
	s_and_b32 s23, s23, 0x7000000
	s_or_b32 s22, s22, s23
	s_lshl_b32 s23, s21, 8
	s_and_b32 s23, s23, 0x100
	s_or_b32 s22, s22, s23
	s_or_b32 s23, s22, 0x4000
	buffer_load_dwordx4 v[10:13], v1, s[4:7], s22 offen sc0 nt
	v_mfma_f32_16x16x32_bf16 v[142:145], v[202:205], v[206:209], v[142:145]
	v_mfma_f32_16x16x32_bf16 v[166:169], v[178:181], v[210:213], v[166:169]
	v_mfma_f32_16x16x32_bf16 v[162:165], v[194:197], v[210:213], v[162:165]
	v_mfma_f32_16x16x32_bf16 v[146:149], v[198:201], v[210:213], v[146:149]
	buffer_load_dwordx4 v[18:21], v1, s[4:7], s23 offen sc0 nt
	s_or_b32 s23, s22, 0x8000
	v_mfma_f32_16x16x32_bf16 v[122:125], v[202:205], v[210:213], v[122:125]
	v_mfma_f32_16x16x32_bf16 v[154:157], v[178:181], v[214:217], v[154:157]
	v_mfma_f32_16x16x32_bf16 v[150:153], v[194:197], v[214:217], v[150:153]
	v_mfma_f32_16x16x32_bf16 v[130:133], v[198:201], v[214:217], v[130:133]
	buffer_load_dwordx4 v[22:25], v1, s[4:7], s23 offen sc0 nt
	s_or_b32 s23, s22, 0xc000
	v_mfma_f32_16x16x32_bf16 v[106:109], v[202:205], v[214:217], v[106:109]
	v_mfma_f32_16x16x32_bf16 v[138:141], v[178:181], v[218:221], v[138:141]
	v_mfma_f32_16x16x32_bf16 v[134:137], v[194:197], v[218:221], v[134:137]
	v_mfma_f32_16x16x32_bf16 v[114:117], v[198:201], v[218:221], v[114:117]
	buffer_load_dwordx4 v[30:33], v1, s[4:7], s23 offen sc0 nt
	s_or_b32 s23, s22, 0x10000
	v_mfma_f32_16x16x32_bf16 v[90:93], v[202:205], v[218:221], v[90:93]
	v_mfma_f32_16x16x32_bf16 v[126:129], v[178:181], v[222:225], v[126:129]
	v_mfma_f32_16x16x32_bf16 v[118:121], v[194:197], v[222:225], v[118:121]
	v_mfma_f32_16x16x32_bf16 v[98:101], v[198:201], v[222:225], v[98:101]
	buffer_load_dwordx4 v[34:37], v1, s[4:7], s23 offen sc0 nt
	s_or_b32 s23, s22, 0x14000
	v_mfma_f32_16x16x32_bf16 v[74:77], v[202:205], v[222:225], v[74:77]
	v_mfma_f32_16x16x32_bf16 v[110:113], v[178:181], v[226:229], v[110:113]
	v_mfma_f32_16x16x32_bf16 v[102:105], v[194:197], v[226:229], v[102:105]
	v_mfma_f32_16x16x32_bf16 v[82:85], v[198:201], v[226:229], v[82:85]
	buffer_load_dwordx4 v[38:41], v1, s[4:7], s23 offen sc0 nt
	s_or_b32 s23, s22, 0x18000
	s_or_b32 s22, s22, 0x1c000
	v_mfma_f32_16x16x32_bf16 v[62:65], v[202:205], v[226:229], v[62:65]
	v_mfma_f32_16x16x32_bf16 v[94:97], v[178:181], v[230:233], v[94:97]
	v_mfma_f32_16x16x32_bf16 v[86:89], v[194:197], v[230:233], v[86:89]
	v_mfma_f32_16x16x32_bf16 v[70:73], v[198:201], v[230:233], v[70:73]
	buffer_load_dwordx4 v[42:45], v1, s[4:7], s23 offen sc0 nt
	v_mfma_f32_16x16x32_bf16 v[54:57], v[202:205], v[230:233], v[54:57]
	v_mfma_f32_16x16x32_bf16 v[78:81], v[178:181], v[234:237], v[78:81]
	v_mfma_f32_16x16x32_bf16 v[66:69], v[194:197], v[234:237], v[66:69]
	v_mfma_f32_16x16x32_bf16 v[58:61], v[198:201], v[234:237], v[58:61]
	buffer_load_dwordx4 v[46:49], v1, s[4:7], s22 offen sc0 nt
	v_mfma_f32_16x16x32_bf16 v[50:53], v[202:205], v[234:237], v[50:53]
	s_waitcnt lgkmcnt(0)
	s_barrier
	ds_read_b128 v[178:181], v182 offset:33792
	ds_read_b128 v[194:197], v182 offset:35840
	ds_read_b128 v[198:201], v182 offset:37888
	ds_read_b128 v[202:205], v182 offset:39936
	ds_read_b128 v[206:209], v238 offset:1024
	ds_read_b128 v[210:213], v238 offset:3072
	ds_read_b128 v[214:217], v238 offset:5120
	ds_read_b128 v[218:221], v238 offset:7168
	ds_read_b128 v[222:225], v238 offset:9216
	ds_read_b128 v[226:229], v238 offset:11264
	ds_read_b128 v[230:233], v238 offset:13312
	ds_read_b128 v[234:237], v238 offset:15360
	v_add_u32_e32 v182, s19, v190
	s_waitcnt vmcnt(11)
	ds_write_b128 v182, v[2:5] offset:32768
	s_waitcnt vmcnt(10)
	ds_write_b128 v182, v[6:9] offset:40960
	s_waitcnt vmcnt(9)
	ds_write_b128 v182, v[14:17] offset:49152
	s_waitcnt vmcnt(8)
	ds_write_b128 v182, v[26:29] offset:57344
	s_waitcnt lgkmcnt(0)
	s_barrier
	v_mfma_f32_16x16x32_bf16 v[174:177], v[178:181], v[206:209], v[174:177]
	s_lshl_b32 s21, s21, 15
	s_and_b32 s21, s21, 0x78000
	s_or_b32 s21, s21, s14
	s_or_b32 s22, s21, 0x2000
	v_mfma_f32_16x16x32_bf16 v[170:173], v[194:197], v[206:209], v[170:173]
	v_mfma_f32_16x16x32_bf16 v[158:161], v[198:201], v[206:209], v[158:161]
	v_mfma_f32_16x16x32_bf16 v[142:145], v[202:205], v[206:209], v[142:145]
	v_mfma_f32_16x16x32_bf16 v[166:169], v[178:181], v[210:213], v[166:169]
	v_mfma_f32_16x16x32_bf16 v[162:165], v[194:197], v[210:213], v[162:165]
	buffer_load_dwordx4 v[2:5], v188, s[0:3], s21 offen sc1
	v_mfma_f32_16x16x32_bf16 v[146:149], v[198:201], v[210:213], v[146:149]
	v_mfma_f32_16x16x32_bf16 v[122:125], v[202:205], v[210:213], v[122:125]
	v_mfma_f32_16x16x32_bf16 v[154:157], v[178:181], v[214:217], v[154:157]
	v_mfma_f32_16x16x32_bf16 v[150:153], v[194:197], v[214:217], v[150:153]
	v_mfma_f32_16x16x32_bf16 v[130:133], v[198:201], v[214:217], v[130:133]
	v_mfma_f32_16x16x32_bf16 v[106:109], v[202:205], v[214:217], v[106:109]
	v_mfma_f32_16x16x32_bf16 v[138:141], v[178:181], v[218:221], v[138:141]
	v_mfma_f32_16x16x32_bf16 v[134:137], v[194:197], v[218:221], v[134:137]
	buffer_load_dwordx4 v[6:9], v188, s[0:3], s22 offen sc1
	s_or_b32 s22, s21, 0x4000
	s_or_b32 s21, s21, 0x6000
	v_mfma_f32_16x16x32_bf16 v[114:117], v[198:201], v[218:221], v[114:117]
	v_mfma_f32_16x16x32_bf16 v[90:93], v[202:205], v[218:221], v[90:93]
	v_mfma_f32_16x16x32_bf16 v[126:129], v[178:181], v[222:225], v[126:129]
	v_mfma_f32_16x16x32_bf16 v[118:121], v[194:197], v[222:225], v[118:121]
	v_mfma_f32_16x16x32_bf16 v[98:101], v[198:201], v[222:225], v[98:101]
	v_mfma_f32_16x16x32_bf16 v[74:77], v[202:205], v[222:225], v[74:77]
	v_mfma_f32_16x16x32_bf16 v[110:113], v[178:181], v[226:229], v[110:113]
	v_mfma_f32_16x16x32_bf16 v[102:105], v[194:197], v[226:229], v[102:105]
	buffer_load_dwordx4 v[14:17], v188, s[0:3], s22 offen sc1
	v_mfma_f32_16x16x32_bf16 v[82:85], v[198:201], v[226:229], v[82:85]
	v_mfma_f32_16x16x32_bf16 v[62:65], v[202:205], v[226:229], v[62:65]
	v_mfma_f32_16x16x32_bf16 v[94:97], v[178:181], v[230:233], v[94:97]
	v_mfma_f32_16x16x32_bf16 v[86:89], v[194:197], v[230:233], v[86:89]
	v_mfma_f32_16x16x32_bf16 v[70:73], v[198:201], v[230:233], v[70:73]
	v_mfma_f32_16x16x32_bf16 v[54:57], v[202:205], v[230:233], v[54:57]
	v_mfma_f32_16x16x32_bf16 v[78:81], v[178:181], v[234:237], v[78:81]
	v_mfma_f32_16x16x32_bf16 v[66:69], v[194:197], v[234:237], v[66:69]
	buffer_load_dwordx4 v[26:29], v188, s[0:3], s21 offen sc1
	v_mfma_f32_16x16x32_bf16 v[58:61], v[198:201], v[234:237], v[58:61]
	v_mfma_f32_16x16x32_bf16 v[50:53], v[202:205], v[234:237], v[50:53]
	s_and_b32 s21, s20, 15
	s_cmp_lg_u32 s21, 15
	s_cbranch_scc1 .LBB1_3
	s_and_b32 s21, s18, 32
	s_add_i32 s21, s21, s12
	s_lshl_b32 s21, s21, 6
	s_and_b32 s21, s21, 0x3f00
	v_add_lshl_u32 v182, v193, s21, 9
	v_add_u32_e32 v206, v184, v182
	buffer_store_dwordx4 v[174:177], v206, s[28:31], 0 offen
	buffer_store_dwordx4 v[170:173], v206, s[28:31], 0 offen offset:64
	buffer_store_dwordx4 v[158:161], v206, s[28:31], 0 offen offset:128
	buffer_store_dwordx4 v[142:145], v206, s[28:31], 0 offen offset:192
	buffer_store_dwordx4 v[166:169], v206, s[28:31], s8 offen
	buffer_store_dwordx4 v[162:165], v206, s[28:31], s8 offen offset:64
	buffer_store_dwordx4 v[146:149], v206, s[28:31], s8 offen offset:128
	buffer_store_dwordx4 v[122:125], v206, s[28:31], s8 offen offset:192
	buffer_store_dwordx4 v[154:157], v206, s[28:31], s15 offen
	buffer_store_dwordx4 v[150:153], v206, s[28:31], s15 offen offset:64
	buffer_store_dwordx4 v[130:133], v206, s[28:31], s15 offen offset:128
	buffer_store_dwordx4 v[106:109], v206, s[28:31], s15 offen offset:192
	buffer_store_dwordx4 v[138:141], v206, s[28:31], s9 offen
	buffer_store_dwordx4 v[134:137], v206, s[28:31], s9 offen offset:64
	buffer_store_dwordx4 v[114:117], v206, s[28:31], s9 offen offset:128
	buffer_store_dwordx4 v[90:93], v206, s[28:31], s9 offen offset:192
	buffer_store_dwordx4 v[126:129], v206, s[28:31], s16 offen
	buffer_store_dwordx4 v[118:121], v206, s[28:31], s16 offen offset:64
	buffer_store_dwordx4 v[98:101], v206, s[28:31], s16 offen offset:128
	buffer_store_dwordx4 v[74:77], v206, s[28:31], s16 offen offset:192
	buffer_store_dwordx4 v[110:113], v206, s[28:31], s10 offen
	buffer_store_dwordx4 v[102:105], v206, s[28:31], s10 offen offset:64
	buffer_store_dwordx4 v[82:85], v206, s[28:31], s10 offen offset:128
	buffer_store_dwordx4 v[62:65], v206, s[28:31], s10 offen offset:192
	buffer_store_dwordx4 v[94:97], v206, s[28:31], s17 offen
	buffer_store_dwordx4 v[86:89], v206, s[28:31], s17 offen offset:64
	buffer_store_dwordx4 v[70:73], v206, s[28:31], s17 offen offset:128
	buffer_store_dwordx4 v[54:57], v206, s[28:31], s17 offen offset:192
	buffer_store_dwordx4 v[78:81], v206, s[28:31], s11 offen
	buffer_store_dwordx4 v[66:69], v206, s[28:31], s11 offen offset:64
	buffer_store_dwordx4 v[58:61], v206, s[28:31], s11 offen offset:128
	buffer_store_dwordx4 v[50:53], v206, s[28:31], s11 offen offset:192
.Lpd_tail:
	s_waitcnt lgkmcnt(0)
	s_barrier
	s_add_i32 s20, s20, 1
	s_add_i32 s18, s18, 2
	v_add_u32_e32 v182, s19, v191
	v_add_u32_e32 v238, s19, v192
	ds_read_b128 v[178:181], v182 offset:32768
	ds_read_b128 v[194:197], v182 offset:34816
	ds_read_b128 v[198:201], v182 offset:36864
	ds_read_b128 v[202:205], v182 offset:38912
	ds_read_b128 v[206:209], v238
	ds_read_b128 v[210:213], v238 offset:2048
	ds_read_b128 v[214:217], v238 offset:4096
	ds_read_b128 v[218:221], v238 offset:6144
	ds_read_b128 v[222:225], v238 offset:8192
	ds_read_b128 v[226:229], v238 offset:10240
	ds_read_b128 v[230:233], v238 offset:12288
	ds_read_b128 v[234:237], v238 offset:14336
	s_min_u32 s21, s20, 29
	s_xor_b32 s19, s19, 0x10000
	v_add_u32_e32 v239, s19, v189
	s_waitcnt vmcnt(43)
	v_cvt_pk_bf16_f32 v13, v12, v13
	v_cvt_pk_bf16_f32 v12, v10, v11
	s_waitcnt vmcnt(42)
	v_cvt_pk_bf16_f32 v11, v20, v21
	v_cvt_pk_bf16_f32 v10, v18, v19
	ds_write2st64_b64 v239, v[12:13], v[10:11] offset1:8
	s_waitcnt vmcnt(41)
	v_cvt_pk_bf16_f32 v11, v24, v25
	v_cvt_pk_bf16_f32 v10, v22, v23
	s_waitcnt vmcnt(40)
	v_cvt_pk_bf16_f32 v13, v32, v33
	v_cvt_pk_bf16_f32 v12, v30, v31
	ds_write2st64_b64 v239, v[10:11], v[12:13] offset0:16 offset1:24
	s_waitcnt vmcnt(39)
	v_cvt_pk_bf16_f32 v11, v36, v37
	v_cvt_pk_bf16_f32 v10, v34, v35
	s_waitcnt vmcnt(38)
	v_cvt_pk_bf16_f32 v13, v40, v41
	v_cvt_pk_bf16_f32 v12, v38, v39
	ds_write2st64_b64 v239, v[10:11], v[12:13] offset0:32 offset1:40
	s_waitcnt vmcnt(37)
	v_cvt_pk_bf16_f32 v11, v44, v45
	v_cvt_pk_bf16_f32 v10, v42, v43
	s_waitcnt vmcnt(36)
	v_cvt_pk_bf16_f32 v13, v48, v49
	v_cvt_pk_bf16_f32 v12, v46, v47
	ds_write2st64_b64 v239, v[10:11], v[12:13] offset0:48 offset1:56
	s_waitcnt lgkmcnt(0)
	s_add_i32 s21, s21, 2
	s_barrier
	v_mfma_f32_16x16x32_bf16 v[174:177], v[178:181], v[206:209], v[240:243]
	s_lshl_b32 s22, s21, 1
	s_and_b32 s22, s22, 0x60
	s_add_i32 s22, s22, s12
	s_lshl_b32 s22, s22, 6
	v_mfma_f32_16x16x32_bf16 v[170:173], v[194:197], v[206:209], v[244:247]
	s_and_b32 s22, s22, 0x3f00
	s_or_b32 s22, s22, s13
	s_lshl_b32 s23, s21, 23
	s_lshl_b32 s22, s22, 9
	v_mfma_f32_16x16x32_bf16 v[158:161], v[198:201], v[206:209], v[248:251]
	s_and_b32 s23, s23, 0x7000000
	s_or_b32 s22, s22, s23
	s_lshl_b32 s23, s21, 8
	s_and_b32 s23, s23, 0x100
	s_or_b32 s22, s22, s23
	s_or_b32 s23, s22, 0x4000
	buffer_load_dwordx4 v[10:13], v1, s[4:7], s22 offen sc0 nt
	v_mfma_f32_16x16x32_bf16 v[142:145], v[202:205], v[206:209], v[252:255]
	v_mfma_f32_16x16x32_bf16 v[166:169], v[178:181], v[210:213], v[240:243]
	v_mfma_f32_16x16x32_bf16 v[162:165], v[194:197], v[210:213], v[244:247]
	v_mfma_f32_16x16x32_bf16 v[146:149], v[198:201], v[210:213], v[248:251]
	buffer_load_dwordx4 v[18:21], v1, s[4:7], s23 offen sc0 nt
	s_or_b32 s23, s22, 0x8000
	v_mfma_f32_16x16x32_bf16 v[122:125], v[202:205], v[210:213], v[252:255]
	v_mfma_f32_16x16x32_bf16 v[154:157], v[178:181], v[214:217], v[240:243]
	v_mfma_f32_16x16x32_bf16 v[150:153], v[194:197], v[214:217], v[244:247]
	v_mfma_f32_16x16x32_bf16 v[130:133], v[198:201], v[214:217], v[248:251]
	buffer_load_dwordx4 v[22:25], v1, s[4:7], s23 offen sc0 nt
	s_or_b32 s23, s22, 0xc000
	v_mfma_f32_16x16x32_bf16 v[106:109], v[202:205], v[214:217], v[252:255]
	v_mfma_f32_16x16x32_bf16 v[138:141], v[178:181], v[218:221], v[240:243]
	v_mfma_f32_16x16x32_bf16 v[134:137], v[194:197], v[218:221], v[244:247]
	v_mfma_f32_16x16x32_bf16 v[114:117], v[198:201], v[218:221], v[248:251]
	buffer_load_dwordx4 v[30:33], v1, s[4:7], s23 offen sc0 nt
	s_or_b32 s23, s22, 0x10000
	v_mfma_f32_16x16x32_bf16 v[90:93], v[202:205], v[218:221], v[252:255]
	v_mfma_f32_16x16x32_bf16 v[126:129], v[178:181], v[222:225], v[240:243]
	v_mfma_f32_16x16x32_bf16 v[118:121], v[194:197], v[222:225], v[244:247]
	v_mfma_f32_16x16x32_bf16 v[98:101], v[198:201], v[222:225], v[248:251]
	buffer_load_dwordx4 v[34:37], v1, s[4:7], s23 offen sc0 nt
	s_or_b32 s23, s22, 0x14000
	v_mfma_f32_16x16x32_bf16 v[74:77], v[202:205], v[222:225], v[252:255]
	v_mfma_f32_16x16x32_bf16 v[110:113], v[178:181], v[226:229], v[240:243]
	v_mfma_f32_16x16x32_bf16 v[102:105], v[194:197], v[226:229], v[244:247]
	v_mfma_f32_16x16x32_bf16 v[82:85], v[198:201], v[226:229], v[248:251]
	buffer_load_dwordx4 v[38:41], v1, s[4:7], s23 offen sc0 nt
	s_or_b32 s23, s22, 0x18000
	s_or_b32 s22, s22, 0x1c000
	v_mfma_f32_16x16x32_bf16 v[62:65], v[202:205], v[226:229], v[252:255]
	v_mfma_f32_16x16x32_bf16 v[94:97], v[178:181], v[230:233], v[240:243]
	v_mfma_f32_16x16x32_bf16 v[86:89], v[194:197], v[230:233], v[244:247]
	v_mfma_f32_16x16x32_bf16 v[70:73], v[198:201], v[230:233], v[248:251]
	buffer_load_dwordx4 v[42:45], v1, s[4:7], s23 offen sc0 nt
	v_mfma_f32_16x16x32_bf16 v[54:57], v[202:205], v[230:233], v[252:255]
	v_mfma_f32_16x16x32_bf16 v[78:81], v[178:181], v[234:237], v[240:243]
	v_mfma_f32_16x16x32_bf16 v[66:69], v[194:197], v[234:237], v[244:247]
	v_mfma_f32_16x16x32_bf16 v[58:61], v[198:201], v[234:237], v[248:251]
	buffer_load_dwordx4 v[46:49], v1, s[4:7], s22 offen sc0 nt
	v_mfma_f32_16x16x32_bf16 v[50:53], v[202:205], v[234:237], v[252:255]
	s_waitcnt lgkmcnt(0)
	s_barrier
	ds_read_b128 v[178:181], v182 offset:33792
	ds_read_b128 v[194:197], v182 offset:35840
	ds_read_b128 v[198:201], v182 offset:37888
	ds_read_b128 v[202:205], v182 offset:39936
	ds_read_b128 v[206:209], v238 offset:1024
	ds_read_b128 v[210:213], v238 offset:3072
	ds_read_b128 v[214:217], v238 offset:5120
	ds_read_b128 v[218:221], v238 offset:7168
	ds_read_b128 v[222:225], v238 offset:9216
	ds_read_b128 v[226:229], v238 offset:11264
	ds_read_b128 v[230:233], v238 offset:13312
	ds_read_b128 v[234:237], v238 offset:15360
	v_add_u32_e32 v182, s19, v190
	s_waitcnt vmcnt(43)
	ds_write_b128 v182, v[2:5] offset:32768
	s_waitcnt vmcnt(42)
	ds_write_b128 v182, v[6:9] offset:40960
	s_waitcnt vmcnt(41)
	ds_write_b128 v182, v[14:17] offset:49152
	s_waitcnt vmcnt(40)
	ds_write_b128 v182, v[26:29] offset:57344
	s_waitcnt lgkmcnt(0)
	s_barrier
	v_mfma_f32_16x16x32_bf16 v[174:177], v[178:181], v[206:209], v[174:177]
	s_lshl_b32 s21, s21, 15
	s_and_b32 s21, s21, 0x78000
	s_or_b32 s21, s21, s14
	s_or_b32 s22, s21, 0x2000
	v_mfma_f32_16x16x32_bf16 v[170:173], v[194:197], v[206:209], v[170:173]
	v_mfma_f32_16x16x32_bf16 v[158:161], v[198:201], v[206:209], v[158:161]
	v_mfma_f32_16x16x32_bf16 v[142:145], v[202:205], v[206:209], v[142:145]
	v_mfma_f32_16x16x32_bf16 v[166:169], v[178:181], v[210:213], v[166:169]
	v_mfma_f32_16x16x32_bf16 v[162:165], v[194:197], v[210:213], v[162:165]
	buffer_load_dwordx4 v[2:5], v188, s[0:3], s21 offen sc1
	v_mfma_f32_16x16x32_bf16 v[146:149], v[198:201], v[210:213], v[146:149]
	v_mfma_f32_16x16x32_bf16 v[122:125], v[202:205], v[210:213], v[122:125]
	v_mfma_f32_16x16x32_bf16 v[154:157], v[178:181], v[214:217], v[154:157]
	v_mfma_f32_16x16x32_bf16 v[150:153], v[194:197], v[214:217], v[150:153]
	v_mfma_f32_16x16x32_bf16 v[130:133], v[198:201], v[214:217], v[130:133]
	v_mfma_f32_16x16x32_bf16 v[106:109], v[202:205], v[214:217], v[106:109]
	v_mfma_f32_16x16x32_bf16 v[138:141], v[178:181], v[218:221], v[138:141]
	v_mfma_f32_16x16x32_bf16 v[134:137], v[194:197], v[218:221], v[134:137]
	buffer_load_dwordx4 v[6:9], v188, s[0:3], s22 offen sc1
	s_or_b32 s22, s21, 0x4000
	s_or_b32 s21, s21, 0x6000
	v_mfma_f32_16x16x32_bf16 v[114:117], v[198:201], v[218:221], v[114:117]
	v_mfma_f32_16x16x32_bf16 v[90:93], v[202:205], v[218:221], v[90:93]
	v_mfma_f32_16x16x32_bf16 v[126:129], v[178:181], v[222:225], v[126:129]
	v_mfma_f32_16x16x32_bf16 v[118:121], v[194:197], v[222:225], v[118:121]
	v_mfma_f32_16x16x32_bf16 v[98:101], v[198:201], v[222:225], v[98:101]
	v_mfma_f32_16x16x32_bf16 v[74:77], v[202:205], v[222:225], v[74:77]
	v_mfma_f32_16x16x32_bf16 v[110:113], v[178:181], v[226:229], v[110:113]
	v_mfma_f32_16x16x32_bf16 v[102:105], v[194:197], v[226:229], v[102:105]
	buffer_load_dwordx4 v[14:17], v188, s[0:3], s22 offen sc1
	v_mfma_f32_16x16x32_bf16 v[82:85], v[198:201], v[226:229], v[82:85]
	v_mfma_f32_16x16x32_bf16 v[62:65], v[202:205], v[226:229], v[62:65]
	v_mfma_f32_16x16x32_bf16 v[94:97], v[178:181], v[230:233], v[94:97]
	v_mfma_f32_16x16x32_bf16 v[86:89], v[194:197], v[230:233], v[86:89]
	v_mfma_f32_16x16x32_bf16 v[70:73], v[198:201], v[230:233], v[70:73]
	v_mfma_f32_16x16x32_bf16 v[54:57], v[202:205], v[230:233], v[54:57]
	v_mfma_f32_16x16x32_bf16 v[78:81], v[178:181], v[234:237], v[78:81]
	v_mfma_f32_16x16x32_bf16 v[66:69], v[194:197], v[234:237], v[66:69]
	buffer_load_dwordx4 v[26:29], v188, s[0:3], s21 offen sc1
	v_mfma_f32_16x16x32_bf16 v[58:61], v[198:201], v[234:237], v[58:61]
	v_mfma_f32_16x16x32_bf16 v[50:53], v[202:205], v[234:237], v[50:53]
	s_branch .LBB1_3
.Lt30:
	v_add_u32_e32 v182, s19, v191
	v_add_u32_e32 v238, s19, v192
	ds_read_b128 v[178:181], v182 offset:32768
	ds_read_b128 v[194:197], v182 offset:34816
	ds_read_b128 v[198:201], v182 offset:36864
	ds_read_b128 v[202:205], v182 offset:38912
	ds_read_b128 v[206:209], v238
	ds_read_b128 v[210:213], v238 offset:2048
	ds_read_b128 v[214:217], v238 offset:4096
	ds_read_b128 v[218:221], v238 offset:6144
	ds_read_b128 v[222:225], v238 offset:8192
	ds_read_b128 v[226:229], v238 offset:10240
	ds_read_b128 v[230:233], v238 offset:12288
	ds_read_b128 v[234:237], v238 offset:14336
	s_min_u32 s21, s20, 29
	s_xor_b32 s19, s19, 0x10000
	v_add_u32_e32 v239, s19, v189
	s_waitcnt vmcnt(11)
	v_cvt_pk_bf16_f32 v13, v12, v13
	v_cvt_pk_bf16_f32 v12, v10, v11
	s_waitcnt vmcnt(10)
	v_cvt_pk_bf16_f32 v11, v20, v21
	v_cvt_pk_bf16_f32 v10, v18, v19
	ds_write2st64_b64 v239, v[12:13], v[10:11] offset1:8
	s_waitcnt vmcnt(9)
	v_cvt_pk_bf16_f32 v11, v24, v25
	v_cvt_pk_bf16_f32 v10, v22, v23
	s_waitcnt vmcnt(8)
	v_cvt_pk_bf16_f32 v13, v32, v33
	v_cvt_pk_bf16_f32 v12, v30, v31
	ds_write2st64_b64 v239, v[10:11], v[12:13] offset0:16 offset1:24
	s_waitcnt vmcnt(7)
	v_cvt_pk_bf16_f32 v11, v36, v37
	v_cvt_pk_bf16_f32 v10, v34, v35
	s_waitcnt vmcnt(6)
	v_cvt_pk_bf16_f32 v13, v40, v41
	v_cvt_pk_bf16_f32 v12, v38, v39
	ds_write2st64_b64 v239, v[10:11], v[12:13] offset0:32 offset1:40
	s_waitcnt vmcnt(5)
	v_cvt_pk_bf16_f32 v11, v44, v45
	v_cvt_pk_bf16_f32 v10, v42, v43
	s_waitcnt vmcnt(4)
	v_cvt_pk_bf16_f32 v13, v48, v49
	v_cvt_pk_bf16_f32 v12, v46, v47
	ds_write2st64_b64 v239, v[10:11], v[12:13] offset0:48 offset1:56
	s_waitcnt lgkmcnt(0)
	s_add_i32 s21, s21, 2
	s_barrier
	v_mfma_f32_16x16x32_bf16 v[174:177], v[178:181], v[206:209], v[174:177]
	s_lshl_b32 s22, s21, 1
	s_and_b32 s22, s22, 0x60
	s_add_i32 s22, s22, s12
	s_lshl_b32 s22, s22, 6
	v_mfma_f32_16x16x32_bf16 v[170:173], v[194:197], v[206:209], v[170:173]
	s_and_b32 s22, s22, 0x3f00
	s_or_b32 s22, s22, s13
	s_lshl_b32 s23, s21, 23
	s_lshl_b32 s22, s22, 9
	v_mfma_f32_16x16x32_bf16 v[158:161], v[198:201], v[206:209], v[158:161]
	s_and_b32 s23, s23, 0x7000000
	s_or_b32 s22, s22, s23
	s_lshl_b32 s23, s21, 8
	s_and_b32 s23, s23, 0x100
	s_or_b32 s22, s22, s23
	s_or_b32 s23, s22, 0x4000
	v_mfma_f32_16x16x32_bf16 v[142:145], v[202:205], v[206:209], v[142:145]
	v_mfma_f32_16x16x32_bf16 v[166:169], v[178:181], v[210:213], v[166:169]
	v_mfma_f32_16x16x32_bf16 v[162:165], v[194:197], v[210:213], v[162:165]
	v_mfma_f32_16x16x32_bf16 v[146:149], v[198:201], v[210:213], v[146:149]
	s_or_b32 s23, s22, 0x8000
	v_mfma_f32_16x16x32_bf16 v[122:125], v[202:205], v[210:213], v[122:125]
	v_mfma_f32_16x16x32_bf16 v[154:157], v[178:181], v[214:217], v[154:157]
	v_mfma_f32_16x16x32_bf16 v[150:153], v[194:197], v[214:217], v[150:153]
	v_mfma_f32_16x16x32_bf16 v[130:133], v[198:201], v[214:217], v[130:133]
	s_or_b32 s23, s22, 0xc000
	v_mfma_f32_16x16x32_bf16 v[106:109], v[202:205], v[214:217], v[106:109]
	v_mfma_f32_16x16x32_bf16 v[138:141], v[178:181], v[218:221], v[138:141]
	v_mfma_f32_16x16x32_bf16 v[134:137], v[194:197], v[218:221], v[134:137]
	v_mfma_f32_16x16x32_bf16 v[114:117], v[198:201], v[218:221], v[114:117]
	s_or_b32 s23, s22, 0x10000
	v_mfma_f32_16x16x32_bf16 v[90:93], v[202:205], v[218:221], v[90:93]
	v_mfma_f32_16x16x32_bf16 v[126:129], v[178:181], v[222:225], v[126:129]
	v_mfma_f32_16x16x32_bf16 v[118:121], v[194:197], v[222:225], v[118:121]
	v_mfma_f32_16x16x32_bf16 v[98:101], v[198:201], v[222:225], v[98:101]
	s_or_b32 s23, s22, 0x14000
	v_mfma_f32_16x16x32_bf16 v[74:77], v[202:205], v[222:225], v[74:77]
	v_mfma_f32_16x16x32_bf16 v[110:113], v[178:181], v[226:229], v[110:113]
	v_mfma_f32_16x16x32_bf16 v[102:105], v[194:197], v[226:229], v[102:105]
	v_mfma_f32_16x16x32_bf16 v[82:85], v[198:201], v[226:229], v[82:85]
	s_or_b32 s23, s22, 0x18000
	s_or_b32 s22, s22, 0x1c000
	v_mfma_f32_16x16x32_bf16 v[62:65], v[202:205], v[226:229], v[62:65]
	v_mfma_f32_16x16x32_bf16 v[94:97], v[178:181], v[230:233], v[94:97]
	v_mfma_f32_16x16x32_bf16 v[86:89], v[194:197], v[230:233], v[86:89]
	v_mfma_f32_16x16x32_bf16 v[70:73], v[198:201], v[230:233], v[70:73]
	v_mfma_f32_16x16x32_bf16 v[54:57], v[202:205], v[230:233], v[54:57]
	v_mfma_f32_16x16x32_bf16 v[78:81], v[178:181], v[234:237], v[78:81]
	v_mfma_f32_16x16x32_bf16 v[66:69], v[194:197], v[234:237], v[66:69]
	v_mfma_f32_16x16x32_bf16 v[58:61], v[198:201], v[234:237], v[58:61]
	v_mfma_f32_16x16x32_bf16 v[50:53], v[202:205], v[234:237], v[50:53]
	s_waitcnt lgkmcnt(0)
	s_barrier
	ds_read_b128 v[178:181], v182 offset:33792
	ds_read_b128 v[194:197], v182 offset:35840
	ds_read_b128 v[198:201], v182 offset:37888
	ds_read_b128 v[202:205], v182 offset:39936
	ds_read_b128 v[206:209], v238 offset:1024
	ds_read_b128 v[210:213], v238 offset:3072
	ds_read_b128 v[214:217], v238 offset:5120
	ds_read_b128 v[218:221], v238 offset:7168
	ds_read_b128 v[222:225], v238 offset:9216
	ds_read_b128 v[226:229], v238 offset:11264
	ds_read_b128 v[230:233], v238 offset:13312
	ds_read_b128 v[234:237], v238 offset:15360
	v_add_u32_e32 v182, s19, v190
	s_waitcnt vmcnt(3)
	ds_write_b128 v182, v[2:5] offset:32768
	s_waitcnt vmcnt(2)
	ds_write_b128 v182, v[6:9] offset:40960
	s_waitcnt vmcnt(1)
	ds_write_b128 v182, v[14:17] offset:49152
	s_waitcnt vmcnt(0)
	ds_write_b128 v182, v[26:29] offset:57344
	s_waitcnt lgkmcnt(0)
	s_barrier
	v_mfma_f32_16x16x32_bf16 v[174:177], v[178:181], v[206:209], v[174:177]
	s_lshl_b32 s21, s21, 15
	s_and_b32 s21, s21, 0x78000
	s_or_b32 s21, s21, s14
	s_or_b32 s22, s21, 0x2000
	v_mfma_f32_16x16x32_bf16 v[170:173], v[194:197], v[206:209], v[170:173]
	v_mfma_f32_16x16x32_bf16 v[158:161], v[198:201], v[206:209], v[158:161]
	v_mfma_f32_16x16x32_bf16 v[142:145], v[202:205], v[206:209], v[142:145]
	v_mfma_f32_16x16x32_bf16 v[166:169], v[178:181], v[210:213], v[166:169]
	v_mfma_f32_16x16x32_bf16 v[162:165], v[194:197], v[210:213], v[162:165]
	v_mfma_f32_16x16x32_bf16 v[146:149], v[198:201], v[210:213], v[146:149]
	v_mfma_f32_16x16x32_bf16 v[122:125], v[202:205], v[210:213], v[122:125]
	v_mfma_f32_16x16x32_bf16 v[154:157], v[178:181], v[214:217], v[154:157]
	v_mfma_f32_16x16x32_bf16 v[150:153], v[194:197], v[214:217], v[150:153]
	v_mfma_f32_16x16x32_bf16 v[130:133], v[198:201], v[214:217], v[130:133]
	v_mfma_f32_16x16x32_bf16 v[106:109], v[202:205], v[214:217], v[106:109]
	v_mfma_f32_16x16x32_bf16 v[138:141], v[178:181], v[218:221], v[138:141]
	v_mfma_f32_16x16x32_bf16 v[134:137], v[194:197], v[218:221], v[134:137]
	s_or_b32 s22, s21, 0x4000
	s_or_b32 s21, s21, 0x6000
	v_mfma_f32_16x16x32_bf16 v[114:117], v[198:201], v[218:221], v[114:117]
	v_mfma_f32_16x16x32_bf16 v[90:93], v[202:205], v[218:221], v[90:93]
	v_mfma_f32_16x16x32_bf16 v[126:129], v[178:181], v[222:225], v[126:129]
	v_mfma_f32_16x16x32_bf16 v[118:121], v[194:197], v[222:225], v[118:121]
	v_mfma_f32_16x16x32_bf16 v[98:101], v[198:201], v[222:225], v[98:101]
	v_mfma_f32_16x16x32_bf16 v[74:77], v[202:205], v[222:225], v[74:77]
	v_mfma_f32_16x16x32_bf16 v[110:113], v[178:181], v[226:229], v[110:113]
	v_mfma_f32_16x16x32_bf16 v[102:105], v[194:197], v[226:229], v[102:105]
	v_mfma_f32_16x16x32_bf16 v[82:85], v[198:201], v[226:229], v[82:85]
	v_mfma_f32_16x16x32_bf16 v[62:65], v[202:205], v[226:229], v[62:65]
	v_mfma_f32_16x16x32_bf16 v[94:97], v[178:181], v[230:233], v[94:97]
	v_mfma_f32_16x16x32_bf16 v[86:89], v[194:197], v[230:233], v[86:89]
	v_mfma_f32_16x16x32_bf16 v[70:73], v[198:201], v[230:233], v[70:73]
	v_mfma_f32_16x16x32_bf16 v[54:57], v[202:205], v[230:233], v[54:57]
	v_mfma_f32_16x16x32_bf16 v[78:81], v[178:181], v[234:237], v[78:81]
	v_mfma_f32_16x16x32_bf16 v[66:69], v[194:197], v[234:237], v[66:69]
	v_mfma_f32_16x16x32_bf16 v[58:61], v[198:201], v[234:237], v[58:61]
	v_mfma_f32_16x16x32_bf16 v[50:53], v[202:205], v[234:237], v[50:53]
	s_waitcnt lgkmcnt(0)
	s_barrier
	s_add_i32 s20, s20, 1
	s_add_i32 s18, s18, 2
	v_add_u32_e32 v182, s19, v191
	v_add_u32_e32 v238, s19, v192
	ds_read_b128 v[178:181], v182 offset:32768
	ds_read_b128 v[194:197], v182 offset:34816
	ds_read_b128 v[198:201], v182 offset:36864
	ds_read_b128 v[202:205], v182 offset:38912
	ds_read_b128 v[206:209], v238
	ds_read_b128 v[210:213], v238 offset:2048
	ds_read_b128 v[214:217], v238 offset:4096
	ds_read_b128 v[218:221], v238 offset:6144
	ds_read_b128 v[222:225], v238 offset:8192
	ds_read_b128 v[226:229], v238 offset:10240
	ds_read_b128 v[230:233], v238 offset:12288
	ds_read_b128 v[234:237], v238 offset:14336
	s_min_u32 s21, s20, 29
	s_xor_b32 s19, s19, 0x10000
	v_add_u32_e32 v239, s19, v189
	s_waitcnt lgkmcnt(0)
	s_add_i32 s21, s21, 2
	s_barrier
	v_mfma_f32_16x16x32_bf16 v[174:177], v[178:181], v[206:209], v[174:177]
	s_lshl_b32 s22, s21, 1
	s_and_b32 s22, s22, 0x60
	s_add_i32 s22, s22, s12
	s_lshl_b32 s22, s22, 6
	v_mfma_f32_16x16x32_bf16 v[170:173], v[194:197], v[206:209], v[170:173]
	s_and_b32 s22, s22, 0x3f00
	s_or_b32 s22, s22, s13
	s_lshl_b32 s23, s21, 23
	s_lshl_b32 s22, s22, 9
	v_mfma_f32_16x16x32_bf16 v[158:161], v[198:201], v[206:209], v[158:161]
	s_and_b32 s23, s23, 0x7000000
	s_or_b32 s22, s22, s23
	s_lshl_b32 s23, s21, 8
	s_and_b32 s23, s23, 0x100
	s_or_b32 s22, s22, s23
	s_or_b32 s23, s22, 0x4000
	v_mfma_f32_16x16x32_bf16 v[142:145], v[202:205], v[206:209], v[142:145]
	v_mfma_f32_16x16x32_bf16 v[166:169], v[178:181], v[210:213], v[166:169]
	v_mfma_f32_16x16x32_bf16 v[162:165], v[194:197], v[210:213], v[162:165]
	v_mfma_f32_16x16x32_bf16 v[146:149], v[198:201], v[210:213], v[146:149]
	s_or_b32 s23, s22, 0x8000
	v_mfma_f32_16x16x32_bf16 v[122:125], v[202:205], v[210:213], v[122:125]
	v_mfma_f32_16x16x32_bf16 v[154:157], v[178:181], v[214:217], v[154:157]
	v_mfma_f32_16x16x32_bf16 v[150:153], v[194:197], v[214:217], v[150:153]
	v_mfma_f32_16x16x32_bf16 v[130:133], v[198:201], v[214:217], v[130:133]
	s_or_b32 s23, s22, 0xc000
	v_mfma_f32_16x16x32_bf16 v[106:109], v[202:205], v[214:217], v[106:109]
	v_mfma_f32_16x16x32_bf16 v[138:141], v[178:181], v[218:221], v[138:141]
	v_mfma_f32_16x16x32_bf16 v[134:137], v[194:197], v[218:221], v[134:137]
	v_mfma_f32_16x16x32_bf16 v[114:117], v[198:201], v[218:221], v[114:117]
	s_or_b32 s23, s22, 0x10000
	v_mfma_f32_16x16x32_bf16 v[90:93], v[202:205], v[218:221], v[90:93]
	v_mfma_f32_16x16x32_bf16 v[126:129], v[178:181], v[222:225], v[126:129]
	v_mfma_f32_16x16x32_bf16 v[118:121], v[194:197], v[222:225], v[118:121]
	v_mfma_f32_16x16x32_bf16 v[98:101], v[198:201], v[222:225], v[98:101]
	s_or_b32 s23, s22, 0x14000
	v_mfma_f32_16x16x32_bf16 v[74:77], v[202:205], v[222:225], v[74:77]
	v_mfma_f32_16x16x32_bf16 v[110:113], v[178:181], v[226:229], v[110:113]
	v_mfma_f32_16x16x32_bf16 v[102:105], v[194:197], v[226:229], v[102:105]
	v_mfma_f32_16x16x32_bf16 v[82:85], v[198:201], v[226:229], v[82:85]
	s_or_b32 s23, s22, 0x18000
	s_or_b32 s22, s22, 0x1c000
	v_mfma_f32_16x16x32_bf16 v[62:65], v[202:205], v[226:229], v[62:65]
	v_mfma_f32_16x16x32_bf16 v[94:97], v[178:181], v[230:233], v[94:97]
	v_mfma_f32_16x16x32_bf16 v[86:89], v[194:197], v[230:233], v[86:89]
	v_mfma_f32_16x16x32_bf16 v[70:73], v[198:201], v[230:233], v[70:73]
	v_mfma_f32_16x16x32_bf16 v[54:57], v[202:205], v[230:233], v[54:57]
	v_mfma_f32_16x16x32_bf16 v[78:81], v[178:181], v[234:237], v[78:81]
	v_mfma_f32_16x16x32_bf16 v[66:69], v[194:197], v[234:237], v[66:69]
	v_mfma_f32_16x16x32_bf16 v[58:61], v[198:201], v[234:237], v[58:61]
	v_mfma_f32_16x16x32_bf16 v[50:53], v[202:205], v[234:237], v[50:53]
	s_waitcnt lgkmcnt(0)
	s_barrier
	ds_read_b128 v[178:181], v182 offset:33792
	ds_read_b128 v[194:197], v182 offset:35840
	ds_read_b128 v[198:201], v182 offset:37888
	ds_read_b128 v[202:205], v182 offset:39936
	ds_read_b128 v[206:209], v238 offset:1024
	ds_read_b128 v[210:213], v238 offset:3072
	ds_read_b128 v[214:217], v238 offset:5120
	ds_read_b128 v[218:221], v238 offset:7168
	ds_read_b128 v[222:225], v238 offset:9216
	ds_read_b128 v[226:229], v238 offset:11264
	ds_read_b128 v[230:233], v238 offset:13312
	ds_read_b128 v[234:237], v238 offset:15360
	s_waitcnt lgkmcnt(0)
	s_barrier
	v_mfma_f32_16x16x32_bf16 v[174:177], v[178:181], v[206:209], v[174:177]
	s_lshl_b32 s21, s21, 15
	s_and_b32 s21, s21, 0x78000
	s_or_b32 s21, s21, s14
	s_or_b32 s22, s21, 0x2000
	v_mfma_f32_16x16x32_bf16 v[170:173], v[194:197], v[206:209], v[170:173]
	v_mfma_f32_16x16x32_bf16 v[158:161], v[198:201], v[206:209], v[158:161]
	v_mfma_f32_16x16x32_bf16 v[142:145], v[202:205], v[206:209], v[142:145]
	v_mfma_f32_16x16x32_bf16 v[166:169], v[178:181], v[210:213], v[166:169]
	v_mfma_f32_16x16x32_bf16 v[162:165], v[194:197], v[210:213], v[162:165]
	v_mfma_f32_16x16x32_bf16 v[146:149], v[198:201], v[210:213], v[146:149]
	v_mfma_f32_16x16x32_bf16 v[122:125], v[202:205], v[210:213], v[122:125]
	v_mfma_f32_16x16x32_bf16 v[154:157], v[178:181], v[214:217], v[154:157]
	v_mfma_f32_16x16x32_bf16 v[150:153], v[194:197], v[214:217], v[150:153]
	v_mfma_f32_16x16x32_bf16 v[130:133], v[198:201], v[214:217], v[130:133]
	v_mfma_f32_16x16x32_bf16 v[106:109], v[202:205], v[214:217], v[106:109]
	v_mfma_f32_16x16x32_bf16 v[138:141], v[178:181], v[218:221], v[138:141]
	v_mfma_f32_16x16x32_bf16 v[134:137], v[194:197], v[218:221], v[134:137]
	s_or_b32 s22, s21, 0x4000
	s_or_b32 s21, s21, 0x6000
	v_mfma_f32_16x16x32_bf16 v[114:117], v[198:201], v[218:221], v[114:117]
	v_mfma_f32_16x16x32_bf16 v[90:93], v[202:205], v[218:221], v[90:93]
	v_mfma_f32_16x16x32_bf16 v[126:129], v[178:181], v[222:225], v[126:129]
	v_mfma_f32_16x16x32_bf16 v[118:121], v[194:197], v[222:225], v[118:121]
	v_mfma_f32_16x16x32_bf16 v[98:101], v[198:201], v[222:225], v[98:101]
	v_mfma_f32_16x16x32_bf16 v[74:77], v[202:205], v[222:225], v[74:77]
	v_mfma_f32_16x16x32_bf16 v[110:113], v[178:181], v[226:229], v[110:113]
	v_mfma_f32_16x16x32_bf16 v[102:105], v[194:197], v[226:229], v[102:105]
	v_mfma_f32_16x16x32_bf16 v[82:85], v[198:201], v[226:229], v[82:85]
	v_mfma_f32_16x16x32_bf16 v[62:65], v[202:205], v[226:229], v[62:65]
	v_mfma_f32_16x16x32_bf16 v[94:97], v[178:181], v[230:233], v[94:97]
	v_mfma_f32_16x16x32_bf16 v[86:89], v[194:197], v[230:233], v[86:89]
	v_mfma_f32_16x16x32_bf16 v[70:73], v[198:201], v[230:233], v[70:73]
	v_mfma_f32_16x16x32_bf16 v[54:57], v[202:205], v[230:233], v[54:57]
	v_mfma_f32_16x16x32_bf16 v[78:81], v[178:181], v[234:237], v[78:81]
	v_mfma_f32_16x16x32_bf16 v[66:69], v[194:197], v[234:237], v[66:69]
	v_mfma_f32_16x16x32_bf16 v[58:61], v[198:201], v[234:237], v[58:61]
	v_mfma_f32_16x16x32_bf16 v[50:53], v[202:205], v[234:237], v[50:53]
	s_and_b32 s21, s18, 32
	s_add_i32 s21, s21, s12
	s_lshl_b32 s21, s21, 6
	s_and_b32 s21, s21, 0x3f00
	v_add_lshl_u32 v182, v193, s21, 9
	v_add_u32_e32 v206, v184, v182
	buffer_store_dwordx4 v[174:177], v206, s[28:31], 0 offen
	buffer_store_dwordx4 v[170:173], v206, s[28:31], 0 offen offset:64
	buffer_store_dwordx4 v[158:161], v206, s[28:31], 0 offen offset:128
	buffer_store_dwordx4 v[142:145], v206, s[28:31], 0 offen offset:192
	buffer_store_dwordx4 v[166:169], v206, s[28:31], s8 offen
	buffer_store_dwordx4 v[162:165], v206, s[28:31], s8 offen offset:64
	buffer_store_dwordx4 v[146:149], v206, s[28:31], s8 offen offset:128
	buffer_store_dwordx4 v[122:125], v206, s[28:31], s8 offen offset:192
	buffer_store_dwordx4 v[154:157], v206, s[28:31], s15 offen
	buffer_store_dwordx4 v[150:153], v206, s[28:31], s15 offen offset:64
	buffer_store_dwordx4 v[130:133], v206, s[28:31], s15 offen offset:128
	buffer_store_dwordx4 v[106:109], v206, s[28:31], s15 offen offset:192
	buffer_store_dwordx4 v[138:141], v206, s[28:31], s9 offen
	buffer_store_dwordx4 v[134:137], v206, s[28:31], s9 offen offset:64
	buffer_store_dwordx4 v[114:117], v206, s[28:31], s9 offen offset:128
	buffer_store_dwordx4 v[90:93], v206, s[28:31], s9 offen offset:192
	buffer_store_dwordx4 v[126:129], v206, s[28:31], s16 offen
	buffer_store_dwordx4 v[118:121], v206, s[28:31], s16 offen offset:64
	buffer_store_dwordx4 v[98:101], v206, s[28:31], s16 offen offset:128
	buffer_store_dwordx4 v[74:77], v206, s[28:31], s16 offen offset:192
	buffer_store_dwordx4 v[110:113], v206, s[28:31], s10 offen
	buffer_store_dwordx4 v[102:105], v206, s[28:31], s10 offen offset:64
	buffer_store_dwordx4 v[82:85], v206, s[28:31], s10 offen offset:128
	buffer_store_dwordx4 v[62:65], v206, s[28:31], s10 offen offset:192
	buffer_store_dwordx4 v[94:97], v206, s[28:31], s17 offen
	buffer_store_dwordx4 v[86:89], v206, s[28:31], s17 offen offset:64
	buffer_store_dwordx4 v[70:73], v206, s[28:31], s17 offen offset:128
	buffer_store_dwordx4 v[54:57], v206, s[28:31], s17 offen offset:192
	buffer_store_dwordx4 v[78:81], v206, s[28:31], s11 offen
	buffer_store_dwordx4 v[66:69], v206, s[28:31], s11 offen offset:64
	buffer_store_dwordx4 v[58:61], v206, s[28:31], s11 offen offset:128
	buffer_store_dwordx4 v[50:53], v206, s[28:31], s11 offen offset:192
	s_waitcnt lgkmcnt(0)
	s_barrier
	s_branch .LBB1_6
.Lfirst:
	v_add_u32_e32 v182, s19, v191
	v_add_u32_e32 v238, s19, v192
	ds_read_b128 v[178:181], v182 offset:32768
	ds_read_b128 v[194:197], v182 offset:34816
	ds_read_b128 v[198:201], v182 offset:36864
	ds_read_b128 v[202:205], v182 offset:38912
	ds_read_b128 v[206:209], v238
	ds_read_b128 v[210:213], v238 offset:2048
	ds_read_b128 v[214:217], v238 offset:4096
	ds_read_b128 v[218:221], v238 offset:6144
	ds_read_b128 v[222:225], v238 offset:8192
	ds_read_b128 v[226:229], v238 offset:10240
	ds_read_b128 v[230:233], v238 offset:12288
	ds_read_b128 v[234:237], v238 offset:14336
	s_min_u32 s21, s20, 29
	s_xor_b32 s19, s19, 0x10000
	v_add_u32_e32 v239, s19, v189
	s_waitcnt vmcnt(11)
	v_cvt_pk_bf16_f32 v13, v12, v13
	v_cvt_pk_bf16_f32 v12, v10, v11
	s_waitcnt vmcnt(10)
	v_cvt_pk_bf16_f32 v11, v20, v21
	v_cvt_pk_bf16_f32 v10, v18, v19
	ds_write2st64_b64 v239, v[12:13], v[10:11] offset1:8
	s_waitcnt vmcnt(9)
	v_cvt_pk_bf16_f32 v11, v24, v25
	v_cvt_pk_bf16_f32 v10, v22, v23
	s_waitcnt vmcnt(8)
	v_cvt_pk_bf16_f32 v13, v32, v33
	v_cvt_pk_bf16_f32 v12, v30, v31
	ds_write2st64_b64 v239, v[10:11], v[12:13] offset0:16 offset1:24
	s_waitcnt vmcnt(7)
	v_cvt_pk_bf16_f32 v11, v36, v37
	v_cvt_pk_bf16_f32 v10, v34, v35
	s_waitcnt vmcnt(6)
	v_cvt_pk_bf16_f32 v13, v40, v41
	v_cvt_pk_bf16_f32 v12, v38, v39
	ds_write2st64_b64 v239, v[10:11], v[12:13] offset0:32 offset1:40
	s_waitcnt vmcnt(5)
	v_cvt_pk_bf16_f32 v11, v44, v45
	v_cvt_pk_bf16_f32 v10, v42, v43
	s_waitcnt vmcnt(4)
	v_cvt_pk_bf16_f32 v13, v48, v49
	v_cvt_pk_bf16_f32 v12, v46, v47
	ds_write2st64_b64 v239, v[10:11], v[12:13] offset0:48 offset1:56
	s_waitcnt lgkmcnt(0)
	s_add_i32 s21, s21, 2
	s_barrier
	v_mfma_f32_16x16x32_bf16 v[174:177], v[178:181], v[206:209], v[240:243]
	s_lshl_b32 s22, s21, 1
	s_and_b32 s22, s22, 0x60
	s_add_i32 s22, s22, s12
	s_lshl_b32 s22, s22, 6
	v_mfma_f32_16x16x32_bf16 v[170:173], v[194:197], v[206:209], v[244:247]
	s_and_b32 s22, s22, 0x3f00
	s_or_b32 s22, s22, s13
	s_lshl_b32 s23, s21, 23
	s_lshl_b32 s22, s22, 9
	v_mfma_f32_16x16x32_bf16 v[158:161], v[198:201], v[206:209], v[248:251]
	s_and_b32 s23, s23, 0x7000000
	s_or_b32 s22, s22, s23
	s_lshl_b32 s23, s21, 8
	s_and_b32 s23, s23, 0x100
	s_or_b32 s22, s22, s23
	s_or_b32 s23, s22, 0x4000
	buffer_load_dwordx4 v[10:13], v1, s[4:7], s22 offen sc0 nt
	v_mfma_f32_16x16x32_bf16 v[142:145], v[202:205], v[206:209], v[252:255]
	v_mfma_f32_16x16x32_bf16 v[166:169], v[178:181], v[210:213], v[240:243]
	v_mfma_f32_16x16x32_bf16 v[162:165], v[194:197], v[210:213], v[244:247]
	v_mfma_f32_16x16x32_bf16 v[146:149], v[198:201], v[210:213], v[248:251]
	buffer_load_dwordx4 v[18:21], v1, s[4:7], s23 offen sc0 nt
	s_or_b32 s23, s22, 0x8000
	v_mfma_f32_16x16x32_bf16 v[122:125], v[202:205], v[210:213], v[252:255]
	v_mfma_f32_16x16x32_bf16 v[154:157], v[178:181], v[214:217], v[240:243]
	v_mfma_f32_16x16x32_bf16 v[150:153], v[194:197], v[214:217], v[244:247]
	v_mfma_f32_16x16x32_bf16 v[130:133], v[198:201], v[214:217], v[248:251]
	buffer_load_dwordx4 v[22:25], v1, s[4:7], s23 offen sc0 nt
	s_or_b32 s23, s22, 0xc000
	v_mfma_f32_16x16x32_bf16 v[106:109], v[202:205], v[214:217], v[252:255]
	v_mfma_f32_16x16x32_bf16 v[138:141], v[178:181], v[218:221], v[240:243]
	v_mfma_f32_16x16x32_bf16 v[134:137], v[194:197], v[218:221], v[244:247]
	v_mfma_f32_16x16x32_bf16 v[114:117], v[198:201], v[218:221], v[248:251]
	buffer_load_dwordx4 v[30:33], v1, s[4:7], s23 offen sc0 nt
	s_or_b32 s23, s22, 0x10000
	v_mfma_f32_16x16x32_bf16 v[90:93], v[202:205], v[218:221], v[252:255]
	v_mfma_f32_16x16x32_bf16 v[126:129], v[178:181], v[222:225], v[240:243]
	v_mfma_f32_16x16x32_bf16 v[118:121], v[194:197], v[222:225], v[244:247]
	v_mfma_f32_16x16x32_bf16 v[98:101], v[198:201], v[222:225], v[248:251]
	buffer_load_dwordx4 v[34:37], v1, s[4:7], s23 offen sc0 nt
	s_or_b32 s23, s22, 0x14000
	v_mfma_f32_16x16x32_bf16 v[74:77], v[202:205], v[222:225], v[252:255]
	v_mfma_f32_16x16x32_bf16 v[110:113], v[178:181], v[226:229], v[240:243]
	v_mfma_f32_16x16x32_bf16 v[102:105], v[194:197], v[226:229], v[244:247]
	v_mfma_f32_16x16x32_bf16 v[82:85], v[198:201], v[226:229], v[248:251]
	buffer_load_dwordx4 v[38:41], v1, s[4:7], s23 offen sc0 nt
	s_or_b32 s23, s22, 0x18000
	s_or_b32 s22, s22, 0x1c000
	v_mfma_f32_16x16x32_bf16 v[62:65], v[202:205], v[226:229], v[252:255]
	v_mfma_f32_16x16x32_bf16 v[94:97], v[178:181], v[230:233], v[240:243]
	v_mfma_f32_16x16x32_bf16 v[86:89], v[194:197], v[230:233], v[244:247]
	v_mfma_f32_16x16x32_bf16 v[70:73], v[198:201], v[230:233], v[248:251]
	buffer_load_dwordx4 v[42:45], v1, s[4:7], s23 offen sc0 nt
	v_mfma_f32_16x16x32_bf16 v[54:57], v[202:205], v[230:233], v[252:255]
	v_mfma_f32_16x16x32_bf16 v[78:81], v[178:181], v[234:237], v[240:243]
	v_mfma_f32_16x16x32_bf16 v[66:69], v[194:197], v[234:237], v[244:247]
	v_mfma_f32_16x16x32_bf16 v[58:61], v[198:201], v[234:237], v[248:251]
	buffer_load_dwordx4 v[46:49], v1, s[4:7], s22 offen sc0 nt
	v_mfma_f32_16x16x32_bf16 v[50:53], v[202:205], v[234:237], v[252:255]
	s_waitcnt lgkmcnt(0)
	s_barrier
	ds_read_b128 v[178:181], v182 offset:33792
	ds_read_b128 v[194:197], v182 offset:35840
	ds_read_b128 v[198:201], v182 offset:37888
	ds_read_b128 v[202:205], v182 offset:39936
	ds_read_b128 v[206:209], v238 offset:1024
	ds_read_b128 v[210:213], v238 offset:3072
	ds_read_b128 v[214:217], v238 offset:5120
	ds_read_b128 v[218:221], v238 offset:7168
	ds_read_b128 v[222:225], v238 offset:9216
	ds_read_b128 v[226:229], v238 offset:11264
	ds_read_b128 v[230:233], v238 offset:13312
	ds_read_b128 v[234:237], v238 offset:15360
	v_add_u32_e32 v182, s19, v190
	s_waitcnt vmcnt(11)
	ds_write_b128 v182, v[2:5] offset:32768
	s_waitcnt vmcnt(10)
	ds_write_b128 v182, v[6:9] offset:40960
	s_waitcnt vmcnt(9)
	ds_write_b128 v182, v[14:17] offset:49152
	s_waitcnt vmcnt(8)
	ds_write_b128 v182, v[26:29] offset:57344
	s_waitcnt lgkmcnt(0)
	s_barrier
	v_mfma_f32_16x16x32_bf16 v[174:177], v[178:181], v[206:209], v[174:177]
	s_lshl_b32 s21, s21, 15
	s_and_b32 s21, s21, 0x78000
	s_or_b32 s21, s21, s14
	s_or_b32 s22, s21, 0x2000
	v_mfma_f32_16x16x32_bf16 v[170:173], v[194:197], v[206:209], v[170:173]
	v_mfma_f32_16x16x32_bf16 v[158:161], v[198:201], v[206:209], v[158:161]
	v_mfma_f32_16x16x32_bf16 v[142:145], v[202:205], v[206:209], v[142:145]
	v_mfma_f32_16x16x32_bf16 v[166:169], v[178:181], v[210:213], v[166:169]
	v_mfma_f32_16x16x32_bf16 v[162:165], v[194:197], v[210:213], v[162:165]
	buffer_load_dwordx4 v[2:5], v188, s[0:3], s21 offen sc1
	v_mfma_f32_16x16x32_bf16 v[146:149], v[198:201], v[210:213], v[146:149]
	v_mfma_f32_16x16x32_bf16 v[122:125], v[202:205], v[210:213], v[122:125]
	v_mfma_f32_16x16x32_bf16 v[154:157], v[178:181], v[214:217], v[154:157]
	v_mfma_f32_16x16x32_bf16 v[150:153], v[194:197], v[214:217], v[150:153]
	v_mfma_f32_16x16x32_bf16 v[130:133], v[198:201], v[214:217], v[130:133]
	v_mfma_f32_16x16x32_bf16 v[106:109], v[202:205], v[214:217], v[106:109]
	v_mfma_f32_16x16x32_bf16 v[138:141], v[178:181], v[218:221], v[138:141]
	v_mfma_f32_16x16x32_bf16 v[134:137], v[194:197], v[218:221], v[134:137]
	buffer_load_dwordx4 v[6:9], v188, s[0:3], s22 offen sc1
	s_or_b32 s22, s21, 0x4000
	s_or_b32 s21, s21, 0x6000
	v_mfma_f32_16x16x32_bf16 v[114:117], v[198:201], v[218:221], v[114:117]
	v_mfma_f32_16x16x32_bf16 v[90:93], v[202:205], v[218:221], v[90:93]
	v_mfma_f32_16x16x32_bf16 v[126:129], v[178:181], v[222:225], v[126:129]
	v_mfma_f32_16x16x32_bf16 v[118:121], v[194:197], v[222:225], v[118:121]
	v_mfma_f32_16x16x32_bf16 v[98:101], v[198:201], v[222:225], v[98:101]
	v_mfma_f32_16x16x32_bf16 v[74:77], v[202:205], v[222:225], v[74:77]
	v_mfma_f32_16x16x32_bf16 v[110:113], v[178:181], v[226:229], v[110:113]
	v_mfma_f32_16x16x32_bf16 v[102:105], v[194:197], v[226:229], v[102:105]
	buffer_load_dwordx4 v[14:17], v188, s[0:3], s22 offen sc1
	v_mfma_f32_16x16x32_bf16 v[82:85], v[198:201], v[226:229], v[82:85]
	v_mfma_f32_16x16x32_bf16 v[62:65], v[202:205], v[226:229], v[62:65]
	v_mfma_f32_16x16x32_bf16 v[94:97], v[178:181], v[230:233], v[94:97]
	v_mfma_f32_16x16x32_bf16 v[86:89], v[194:197], v[230:233], v[86:89]
	v_mfma_f32_16x16x32_bf16 v[70:73], v[198:201], v[230:233], v[70:73]
	v_mfma_f32_16x16x32_bf16 v[54:57], v[202:205], v[230:233], v[54:57]
	v_mfma_f32_16x16x32_bf16 v[78:81], v[178:181], v[234:237], v[78:81]
	v_mfma_f32_16x16x32_bf16 v[66:69], v[194:197], v[234:237], v[66:69]
	buffer_load_dwordx4 v[26:29], v188, s[0:3], s21 offen sc1
	v_mfma_f32_16x16x32_bf16 v[58:61], v[198:201], v[234:237], v[58:61]
	v_mfma_f32_16x16x32_bf16 v[50:53], v[202:205], v[234:237], v[50:53]
	s_branch .LBB1_3
